# P7 epilogue: list2 row indices fetched during last K sub-phase instead of at epilogue start
# baseline (speedup 1.0000x reference)
; #define PG8_STAGE(bufoff, gbase, voff) do { _Pragma("unroll") for (int _i = 0; _i < 2; ++_i) { unsigned keep_; \
;         asm volatile("s_mov_b32 %0, m0\n\ts_mov_b32 m0, %3\n\ts_nop 0\n\tglobal_load_lds_dwordx4 %1, %2\n\ts_mov_b32 m0, %0" : "=&s"(keep_) : "v"((voff)[_i]), "s"((const char*)(gbase)), "s"(ldsb + (unsigned)((bufoff) + _i * 8192)) : "memory"); } } while (0)
; #define PG8_LDA(dst, b, h) do { _Pragma("unroll") for (int m = 0; m < 4; ++m) _Pragma("unroll") for (int k = 0; k < 2; ++k) dst[m][k] = *(const PG8_LAS bf16x8*)(lds + PG8_SA(b, h) + aoff + m * 2048 + k * 1024); } while (0)
; #define PG8_LDB(dst, b, h) do { _Pragma("unroll") for (int n = 0; n < 2; ++n) _Pragma("unroll") for (int k = 0; k < 2; ++k) dst[n][k] = *(const PG8_LAS bf16x8*)(lds + PG8_SB(b, h) + boff + n * 2048 + k * 1024); } while (0)
; #define PG8_WAIT_V(n) asm volatile("s_waitcnt vmcnt(" #n ")" ::: "memory")
; #define PG8_WAIT_L(n) asm volatile("s_waitcnt lgkmcnt(" #n ")" ::: "memory")
; #define PG8_BAR __builtin_amdgcn_s_barrier()
; #define PG8_SCHED __builtin_amdgcn_sched_barrier(0)
; template <class Epi, class Sched, bool ALIGN_EPI, bool FP8 = false>
; __device__ __forceinline__ void gemm_phase(PG8_LAS unsigned char* lds, const Gemm g, const Sched& S, const Epi& E, const int wid, const int lane) {
;     ...
;         for (int t = 0; t < nt; t += 2) {
;             const bool last = (t == nt - 2);
;             const char* a1 = cA + (size_t)(t + 1) * kstep;
;             const char* a2 = last ? nA : cA + (size_t)(t + 2) * kstep; const char* b2 = last ? nB : cB + (size_t)(t + 2) * kstep;
;             const char* a3 = a2 + kstep; const char* b3 = b2 + kstep;
;             PG8_LDB(B0, 0, 0); PG8_LDB(B1, 0, 1); PG8_SCHED; PG8_LDA(At, 0, 0); PG8_STAGE(PG8_SA(1, 1), a1 + hstepA, vc1);
;             if (GA && last && has_next) { const u32x4 q = *gslot; vc0[0] = q.x; vc0[1] = q.y; vc1[0] = q.z; vc1[1] = q.w; }
;             PG8_WAIT_V(8); PG8_WAIT_L(0); PG8_BAR; PG8_MMA(0, 0, At, B0); PG8_MMA(0, 1, At, B1); PG8_BAR; PG8_SCHED;
;             PG8_LDA(At, 0, 1); PG8_STAGE(PG8_SB(0, 0), b2, voffB); PG8_STAGE(PG8_SB(0, 1), b2 + hstep, voffB); PG8_STAGE(PG8_SA(0, 0), a2, vc0);
;             PG8_WAIT_V(8); PG8_WAIT_L(0); PG8_BAR; PG8_MMA(1, 0, At, B0); PG8_MMA(1, 1, At, B1); PG8_BAR; PG8_SCHED;
.LBB0_852:
	ds_read_b128 v[24:27], v165
	ds_read_b128 v[28:31], v165 offset:1024
	ds_read_b128 v[16:19], v165 offset:2048
	ds_read_b128 v[20:23], v165 offset:3072
	ds_read_b128 v[8:11], v167
	ds_read_b128 v[12:15], v167 offset:1024
	ds_read_b128 v[0:3], v167 offset:2048
	ds_read_b128 v[4:7], v167 offset:3072
	s_add_i32 s33, s8, 2
	s_cmp_eq_u32 s67, s8
	s_cselect_b32 s36, s28, s75
	s_cselect_b32 s37, s29, s82
	s_cselect_b32 s34, s30, s83
	s_cselect_b32 s35, s31, s84
	s_add_u32 s8, s36, 0x80
	s_addc_u32 s9, s37, 0
	ds_read_b128 v[174:177], v169
	ds_read_b128 v[178:181], v169 offset:1024
	ds_read_b128 v[182:185], v169 offset:2048
	ds_read_b128 v[186:189], v169 offset:3072
	ds_read_b128 v[190:193], v169 offset:4096
	ds_read_b128 v[194:197], v169 offset:5120
	ds_read_b128 v[198:201], v169 offset:6144
	ds_read_b128 v[202:205], v169 offset:7168
	s_mov_b32 m0, s68
	s_nop 0
	global_load_lds_dwordx4 v160, s[6:7]
	s_mov_b32 m0, s69
	s_nop 0
	global_load_lds_dwordx4 v164, s[6:7]
	s_waitcnt vmcnt(8)
	s_waitcnt lgkmcnt(0)
	s_barrier
	s_setprio 1
	s_waitcnt lgkmcnt(6)
	v_mfma_scale_f32_16x16x128_f8f6f4 v[156:159], v[24:31], v[174:181], v[156:159], v170, v171 op_sel_hi:[0,0,0]
	v_mfma_scale_f32_16x16x128_f8f6f4 v[152:155], v[16:23], v[174:181], v[152:155], v170, v171 op_sel_hi:[0,0,0]
	s_waitcnt lgkmcnt(4)
	v_mfma_scale_f32_16x16x128_f8f6f4 v[140:143], v[24:31], v[182:189], v[140:143], v170, v171 op_sel_hi:[0,0,0]
	v_mfma_scale_f32_16x16x128_f8f6f4 v[136:139], v[16:23], v[182:189], v[136:139], v170, v171 op_sel_hi:[0,0,0]
	s_waitcnt lgkmcnt(2)
	v_mfma_scale_f32_16x16x128_f8f6f4 v[124:127], v[24:31], v[190:197], v[124:127], v170, v171 op_sel_hi:[0,0,0]
	v_mfma_scale_f32_16x16x128_f8f6f4 v[120:123], v[16:23], v[190:197], v[120:123], v170, v171 op_sel_hi:[0,0,0]
	s_waitcnt lgkmcnt(0)
	v_mfma_scale_f32_16x16x128_f8f6f4 v[108:111], v[24:31], v[198:205], v[108:111], v170, v171 op_sel_hi:[0,0,0]
	v_mfma_scale_f32_16x16x128_f8f6f4 v[104:107], v[16:23], v[198:205], v[104:107], v170, v171 op_sel_hi:[0,0,0]
	s_setprio 0
	s_setprio 1
	v_mfma_scale_f32_16x16x128_f8f6f4 v[148:151], v[8:15], v[174:181], v[148:151], v170, v171 op_sel_hi:[0,0,0]
	v_mfma_scale_f32_16x16x128_f8f6f4 v[144:147], v[0:7], v[174:181], v[144:147], v170, v171 op_sel_hi:[0,0,0]
	v_mfma_scale_f32_16x16x128_f8f6f4 v[132:135], v[8:15], v[182:189], v[132:135], v170, v171 op_sel_hi:[0,0,0]
	v_mfma_scale_f32_16x16x128_f8f6f4 v[128:131], v[0:7], v[182:189], v[128:131], v170, v171 op_sel_hi:[0,0,0]
	v_mfma_scale_f32_16x16x128_f8f6f4 v[116:119], v[8:15], v[190:197], v[116:119], v170, v171 op_sel_hi:[0,0,0]
	v_mfma_scale_f32_16x16x128_f8f6f4 v[112:115], v[0:7], v[190:197], v[112:115], v170, v171 op_sel_hi:[0,0,0]
	v_mfma_scale_f32_16x16x128_f8f6f4 v[100:103], v[8:15], v[198:205], v[100:103], v170, v171 op_sel_hi:[0,0,0]
	v_mfma_scale_f32_16x16x128_f8f6f4 v[96:99], v[0:7], v[198:205], v[96:99], v170, v171 op_sel_hi:[0,0,0]
	s_setprio 0
	s_barrier
	ds_read_b128 v[174:177], v169 offset:16384
	ds_read_b128 v[178:181], v169 offset:17408
	ds_read_b128 v[182:185], v169 offset:18432
	ds_read_b128 v[186:189], v169 offset:19456
	ds_read_b128 v[190:193], v169 offset:20480
	ds_read_b128 v[194:197], v169 offset:21504
	ds_read_b128 v[198:201], v169 offset:22528
	ds_read_b128 v[202:205], v169 offset:23552
	s_mov_b32 m0, s45
	s_nop 0
	global_load_lds_dwordx4 v162, s[34:35]
	s_mov_b32 m0, s46
	s_nop 0
	global_load_lds_dwordx4 v166, s[34:35]
	s_add_u32 s58, s34, s12
	s_addc_u32 s59, s35, s13
	s_mov_b32 m0, s47
	s_nop 0
	global_load_lds_dwordx4 v162, s[58:59]
	s_mov_b32 m0, s48
	s_nop 0
	global_load_lds_dwordx4 v166, s[58:59]
	s_mov_b32 m0, s40
	s_nop 0
	global_load_lds_dwordx4 v160, s[36:37]
	s_mov_b32 m0, s49
	s_nop 0
	global_load_lds_dwordx4 v164, s[36:37]
	s_waitcnt vmcnt(8)
	s_waitcnt lgkmcnt(0)
	s_barrier
	s_setprio 1
	s_waitcnt lgkmcnt(6)
	v_mfma_scale_f32_16x16x128_f8f6f4 v[92:95], v[24:31], v[174:181], v[92:95], v170, v171 op_sel_hi:[0,0,0]
	v_mfma_scale_f32_16x16x128_f8f6f4 v[88:91], v[16:23], v[174:181], v[88:91], v170, v171 op_sel_hi:[0,0,0]
	s_waitcnt lgkmcnt(4)
	v_mfma_scale_f32_16x16x128_f8f6f4 v[76:79], v[24:31], v[182:189], v[76:79], v170, v171 op_sel_hi:[0,0,0]
	v_mfma_scale_f32_16x16x128_f8f6f4 v[72:75], v[16:23], v[182:189], v[72:75], v170, v171 op_sel_hi:[0,0,0]
	s_waitcnt lgkmcnt(2)
	v_mfma_scale_f32_16x16x128_f8f6f4 v[60:63], v[24:31], v[190:197], v[60:63], v170, v171 op_sel_hi:[0,0,0]
	v_mfma_scale_f32_16x16x128_f8f6f4 v[56:59], v[16:23], v[190:197], v[56:59], v170, v171 op_sel_hi:[0,0,0]
	s_waitcnt lgkmcnt(0)
	v_mfma_scale_f32_16x16x128_f8f6f4 v[44:47], v[24:31], v[198:205], v[44:47], v170, v171 op_sel_hi:[0,0,0]
	v_mfma_scale_f32_16x16x128_f8f6f4 v[40:43], v[16:23], v[198:205], v[40:43], v170, v171 op_sel_hi:[0,0,0]
	s_setprio 0
	s_setprio 1
	v_mfma_scale_f32_16x16x128_f8f6f4 v[84:87], v[8:15], v[174:181], v[84:87], v170, v171 op_sel_hi:[0,0,0]
	v_mfma_scale_f32_16x16x128_f8f6f4 v[80:83], v[0:7], v[174:181], v[80:83], v170, v171 op_sel_hi:[0,0,0]
	v_mfma_scale_f32_16x16x128_f8f6f4 v[68:71], v[8:15], v[182:189], v[68:71], v170, v171 op_sel_hi:[0,0,0]
	v_mfma_scale_f32_16x16x128_f8f6f4 v[64:67], v[0:7], v[182:189], v[64:67], v170, v171 op_sel_hi:[0,0,0]
	v_mfma_scale_f32_16x16x128_f8f6f4 v[52:55], v[8:15], v[190:197], v[52:55], v170, v171 op_sel_hi:[0,0,0]
	v_mfma_scale_f32_16x16x128_f8f6f4 v[48:51], v[0:7], v[190:197], v[48:51], v170, v171 op_sel_hi:[0,0,0]
	v_mfma_scale_f32_16x16x128_f8f6f4 v[36:39], v[8:15], v[198:205], v[36:39], v170, v171 op_sel_hi:[0,0,0]
	v_mfma_scale_f32_16x16x128_f8f6f4 v[32:35], v[0:7], v[198:205], v[32:35], v170, v171 op_sel_hi:[0,0,0]
	s_setprio 0
	s_barrier
; #define PG8_STAGE(bufoff, gbase, voff) do { _Pragma("unroll") for (int _i = 0; _i < 2; ++_i) { unsigned keep_; \
;         asm volatile("s_mov_b32 %0, m0\n\ts_mov_b32 m0, %3\n\ts_nop 0\n\tglobal_load_lds_dwordx4 %1, %2\n\ts_mov_b32 m0, %0" : "=&s"(keep_) : "v"((voff)[_i]), "s"((const char*)(gbase)), "s"(ldsb + (unsigned)((bufoff) + _i * 8192)) : "memory"); } } while (0)
; #define PG8_LDA(dst, b, h) do { _Pragma("unroll") for (int m = 0; m < 4; ++m) _Pragma("unroll") for (int k = 0; k < 2; ++k) dst[m][k] = *(const PG8_LAS bf16x8*)(lds + PG8_SA(b, h) + aoff + m * 2048 + k * 1024); } while (0)
; #define PG8_LDB(dst, b, h) do { _Pragma("unroll") for (int n = 0; n < 2; ++n) _Pragma("unroll") for (int k = 0; k < 2; ++k) dst[n][k] = *(const PG8_LAS bf16x8*)(lds + PG8_SB(b, h) + boff + n * 2048 + k * 1024); } while (0)
; #define PG8_WAIT_V(n) asm volatile("s_waitcnt vmcnt(" #n ")" ::: "memory")
; #define PG8_WAIT_L(n) asm volatile("s_waitcnt lgkmcnt(" #n ")" ::: "memory")
; #define PG8_BAR __builtin_amdgcn_s_barrier()
; #define PG8_SCHED __builtin_amdgcn_sched_barrier(0)
; template <class Epi, class Sched, bool ALIGN_EPI, bool FP8 = false>
; __device__ __forceinline__ void gemm_phase(PG8_LAS unsigned char* lds, const Gemm g, const Sched& S, const Epi& E, const int wid, const int lane) {
;     ...
;             PG8_LDB(B0, 1, 0); PG8_LDB(B1, 1, 1); PG8_SCHED; PG8_LDA(At, 1, 0); PG8_STAGE(PG8_SA(0, 1), a2 + hstepA, vc1);
;             PG8_WAIT_V(8); PG8_WAIT_L(0); PG8_BAR; PG8_MMA(0, 0, At, B0); PG8_MMA(0, 1, At, B1); PG8_BAR; PG8_SCHED;
;             PG8_LDA(At, 1, 1); PG8_STAGE(PG8_SB(1, 0), b3, voffB); PG8_STAGE(PG8_SB(1, 1), b3 + hstep, voffB); PG8_STAGE(PG8_SA(1, 0), a3, vc0);
;     __device__ __forceinline__ void operator()(const f32x4 (&acc)[2][2][4][2], const Unit& u, int wr, int wc, int fr, int fq) const {
;         const int col0 = (u.pn & 7) * 256 + wc * 64 + 16 * fq;
;         const int e = tileE[u.pm], lbase = (u.pm - tb[e]) * 256 + wr * 64 + fr, ce = cnt[e];
;         const float ysc = (float)(1 << YSHIFT);
;         int drow[2][4];
; #pragma unroll
;         for (int ai = 0; ai < 2; ++ai)
; #pragma unroll
;             for (int m = 0; m < 4; ++m) { const int local = lbase + ai * HALF + m * 16; drow[ai][m] = (e >= NE) ? (local * 7 + 6) : ((local < ce) ? list2[(size_t)e * LISTCAP + local] : 7 * T); }
	ds_read_b128 v[0:3], v172
	ds_read_b128 v[4:7], v172 offset:1024
	ds_read_b128 v[8:11], v172 offset:2048
	ds_read_b128 v[12:15], v172 offset:3072
	ds_read_b128 v[16:19], v173
	ds_read_b128 v[20:23], v173 offset:1024
	ds_read_b128 v[24:27], v173 offset:2048
	ds_read_b128 v[28:31], v173 offset:3072
	ds_read_b128 v[174:177], v169 offset:32768
	ds_read_b128 v[178:181], v169 offset:33792
	ds_read_b128 v[182:185], v169 offset:34816
	ds_read_b128 v[186:189], v169 offset:35840
	ds_read_b128 v[190:193], v169 offset:36864
	ds_read_b128 v[194:197], v169 offset:37888
	ds_read_b128 v[198:201], v169 offset:38912
	ds_read_b128 v[202:205], v169 offset:39936
	s_add_u32 s36, s36, s12
	s_addc_u32 s37, s37, s13
	s_mov_b32 m0, s50
	s_nop 0
	global_load_lds_dwordx4 v160, s[36:37]
	s_mov_b32 m0, s51
	s_nop 0
	global_load_lds_dwordx4 v164, s[36:37]
	s_waitcnt vmcnt(8)
	s_waitcnt lgkmcnt(0)
	s_barrier
	s_setprio 1
	s_waitcnt lgkmcnt(6)
	v_mfma_scale_f32_16x16x128_f8f6f4 v[156:159], v[0:7], v[174:181], v[156:159], v170, v171 op_sel_hi:[0,0,0]
	v_mfma_scale_f32_16x16x128_f8f6f4 v[152:155], v[8:15], v[174:181], v[152:155], v170, v171 op_sel_hi:[0,0,0]
	s_waitcnt lgkmcnt(4)
	v_mfma_scale_f32_16x16x128_f8f6f4 v[140:143], v[0:7], v[182:189], v[140:143], v170, v171 op_sel_hi:[0,0,0]
	v_mfma_scale_f32_16x16x128_f8f6f4 v[136:139], v[8:15], v[182:189], v[136:139], v170, v171 op_sel_hi:[0,0,0]
	s_waitcnt lgkmcnt(2)
	v_mfma_scale_f32_16x16x128_f8f6f4 v[124:127], v[0:7], v[190:197], v[124:127], v170, v171 op_sel_hi:[0,0,0]
	v_mfma_scale_f32_16x16x128_f8f6f4 v[120:123], v[8:15], v[190:197], v[120:123], v170, v171 op_sel_hi:[0,0,0]
	s_waitcnt lgkmcnt(0)
	v_mfma_scale_f32_16x16x128_f8f6f4 v[108:111], v[0:7], v[198:205], v[108:111], v170, v171 op_sel_hi:[0,0,0]
	v_mfma_scale_f32_16x16x128_f8f6f4 v[104:107], v[8:15], v[198:205], v[104:107], v170, v171 op_sel_hi:[0,0,0]
	s_setprio 0
	s_setprio 1
	v_mfma_scale_f32_16x16x128_f8f6f4 v[148:151], v[16:23], v[174:181], v[148:151], v170, v171 op_sel_hi:[0,0,0]
	v_mfma_scale_f32_16x16x128_f8f6f4 v[144:147], v[24:31], v[174:181], v[144:147], v170, v171 op_sel_hi:[0,0,0]
	v_mfma_scale_f32_16x16x128_f8f6f4 v[132:135], v[16:23], v[182:189], v[132:135], v170, v171 op_sel_hi:[0,0,0]
	v_mfma_scale_f32_16x16x128_f8f6f4 v[128:131], v[24:31], v[182:189], v[128:131], v170, v171 op_sel_hi:[0,0,0]
	v_mfma_scale_f32_16x16x128_f8f6f4 v[116:119], v[16:23], v[190:197], v[116:119], v170, v171 op_sel_hi:[0,0,0]
	v_mfma_scale_f32_16x16x128_f8f6f4 v[112:115], v[24:31], v[190:197], v[112:115], v170, v171 op_sel_hi:[0,0,0]
	v_mfma_scale_f32_16x16x128_f8f6f4 v[100:103], v[16:23], v[198:205], v[100:103], v170, v171 op_sel_hi:[0,0,0]
	v_mfma_scale_f32_16x16x128_f8f6f4 v[96:99], v[24:31], v[198:205], v[96:99], v170, v171 op_sel_hi:[0,0,0]
	s_setprio 0
	s_barrier
	ds_read_b128 v[174:177], v169 offset:49152
	ds_read_b128 v[178:181], v169 offset:50176
	ds_read_b128 v[182:185], v169 offset:51200
	ds_read_b128 v[186:189], v169 offset:52224
	ds_read_b128 v[190:193], v169 offset:53248
	ds_read_b128 v[194:197], v169 offset:54272
	ds_read_b128 v[198:201], v169 offset:55296
	ds_read_b128 v[202:205], v169 offset:56320
	s_add_u32 s34, s34, 0x80
	s_addc_u32 s35, s35, 0
	s_mov_b32 m0, s53
	s_nop 0
	global_load_lds_dwordx4 v162, s[34:35]
	s_mov_b32 m0, s54
	s_nop 0
	global_load_lds_dwordx4 v166, s[34:35]
	s_add_u32 s34, s34, s12
	s_addc_u32 s35, s35, s13
	s_mov_b32 m0, s65
	s_nop 0
	global_load_lds_dwordx4 v162, s[34:35]
	s_mov_b32 m0, s66
	s_nop 0
	global_load_lds_dwordx4 v166, s[34:35]
	s_mov_b32 m0, s55
	s_nop 0
	global_load_lds_dwordx4 v160, s[8:9]
	s_mov_b32 m0, s64
	s_nop 0
	global_load_lds_dwordx4 v164, s[8:9]
	s_waitcnt vmcnt(8)
	s_waitcnt lgkmcnt(0)
	s_cmp_lt_i32 s33, s52
	s_cbranch_scc1 .Lp7a_skip
	s_lshl_b32 s98, s74, 2
	s_add_i32 s98, s98, 0x20800
	v_mov_b32_e32 v206, s98
	ds_read_b32 v207, v206
	s_waitcnt lgkmcnt(0)
	s_nop 0
	v_readfirstlane_b32 s99, v207
	s_nop 3
	s_lshl_b32 s98, s99, 2
	s_add_i32 s100, s98, 0x21000
	s_add_i32 s98, s98, 0x21200
	v_mov_b32_e32 v206, s100
	v_mov_b32_e32 v207, s98
	ds_read_b32 v206, v206
	ds_read_b32 v207, v207
	s_waitcnt lgkmcnt(0)
	v_sub_u32_e32 v206, s74, v206
	v_lshl_add_u32 v208, v206, 8, v161
	s_cmp_gt_i32 s99, 63
	s_cbranch_scc1 .Lp7a_shared
	s_mov_b32 s100, s99
	s_ashr_i32 s101, s99, 31
	s_lshl_b64 s[100:101], s[100:101], 16
	s_add_u32 s100, s20, s100
	s_addc_u32 s101, s21, s101
	v_add_u32_e32 v209, 0, v208
	v_cmp_lt_i32_e32 vcc, v209, v207
	v_lshlrev_b32_e32 v238, 2, v209
	v_mov_b32_e32 v230, 0x1c000
	s_and_saveexec_b64 s[98:99], vcc
	s_cbranch_execz .Lp7a_g0
	global_load_dword v230, v238, s[100:101]
; #define PG8_WAIT_V(n) asm volatile("s_waitcnt vmcnt(" #n ")" ::: "memory")
; #define PG8_WAIT_L(n) asm volatile("s_waitcnt lgkmcnt(" #n ")" ::: "memory")
; #define PG8_BAR __builtin_amdgcn_s_barrier()
; #define PG8_SCHED __builtin_amdgcn_sched_barrier(0)
; template <class Epi, class Sched, bool ALIGN_EPI, bool FP8 = false>
; __device__ __forceinline__ void gemm_phase(PG8_LAS unsigned char* lds, const Gemm g, const Sched& S, const Epi& E, const int wid, const int lane) {
;     ...
;             PG8_WAIT_V(8); PG8_WAIT_L(0); PG8_BAR; PG8_MMA(1, 0, At, B0); PG8_MMA(1, 1, At, B1); PG8_BAR; PG8_SCHED;
;     __device__ __forceinline__ void operator()(const f32x4 (&acc)[2][2][4][2], const Unit& u, int wr, int wc, int fr, int fq) const {
;     ...
;             for (int m = 0; m < 4; ++m) { const int local = lbase + ai * HALF + m * 16; drow[ai][m] = (e >= NE) ? (local * 7 + 6) : ((local < ce) ? list2[(size_t)e * LISTCAP + local] : 7 * T); }
.Lp7a_g0:
	s_or_b64 exec, exec, s[98:99]
	v_add_u32_e32 v209, 16, v208
	v_cmp_lt_i32_e32 vcc, v209, v207
	v_lshlrev_b32_e32 v239, 2, v209
	v_mov_b32_e32 v231, 0x1c000
	s_and_saveexec_b64 s[98:99], vcc
	s_cbranch_execz .Lp7a_g1
	global_load_dword v231, v239, s[100:101]
.Lp7a_g1:
	s_or_b64 exec, exec, s[98:99]
	v_add_u32_e32 v209, 32, v208
	v_cmp_lt_i32_e32 vcc, v209, v207
	v_lshlrev_b32_e32 v240, 2, v209
	v_mov_b32_e32 v232, 0x1c000
	s_and_saveexec_b64 s[98:99], vcc
	s_cbranch_execz .Lp7a_g2
	global_load_dword v232, v240, s[100:101]
.Lp7a_g2:
	s_or_b64 exec, exec, s[98:99]
	v_add_u32_e32 v209, 48, v208
	v_cmp_lt_i32_e32 vcc, v209, v207
	v_lshlrev_b32_e32 v241, 2, v209
	v_mov_b32_e32 v233, 0x1c000
	s_and_saveexec_b64 s[98:99], vcc
	s_cbranch_execz .Lp7a_g3
	global_load_dword v233, v241, s[100:101]
.Lp7a_g3:
	s_or_b64 exec, exec, s[98:99]
	v_add_u32_e32 v209, 0x80, v208
	v_cmp_lt_i32_e32 vcc, v209, v207
	v_lshlrev_b32_e32 v242, 2, v209
	v_mov_b32_e32 v234, 0x1c000
	s_and_saveexec_b64 s[98:99], vcc
	s_cbranch_execz .Lp7a_g4
	global_load_dword v234, v242, s[100:101]
.Lp7a_g4:
	s_or_b64 exec, exec, s[98:99]
	v_add_u32_e32 v209, 0x90, v208
	v_cmp_lt_i32_e32 vcc, v209, v207
	v_lshlrev_b32_e32 v243, 2, v209
	v_mov_b32_e32 v235, 0x1c000
	s_and_saveexec_b64 s[98:99], vcc
	s_cbranch_execz .Lp7a_g5
	global_load_dword v235, v243, s[100:101]
.Lp7a_g5:
	s_or_b64 exec, exec, s[98:99]
	v_add_u32_e32 v209, 0xa0, v208
	v_cmp_lt_i32_e32 vcc, v209, v207
	v_lshlrev_b32_e32 v244, 2, v209
	v_mov_b32_e32 v236, 0x1c000
	s_and_saveexec_b64 s[98:99], vcc
	s_cbranch_execz .Lp7a_g6
	global_load_dword v236, v244, s[100:101]
.Lp7a_g6:
	s_or_b64 exec, exec, s[98:99]
	v_add_u32_e32 v209, 0xb0, v208
	v_cmp_lt_i32_e32 vcc, v209, v207
	v_lshlrev_b32_e32 v245, 2, v209
	v_mov_b32_e32 v237, 0x1c000
	s_and_saveexec_b64 s[98:99], vcc
	s_cbranch_execz .Lp7a_g7
	global_load_dword v237, v245, s[100:101]
.Lp7a_g7:
	s_or_b64 exec, exec, s[98:99]
	s_branch .Lp7a_skip
.Lp7a_shared:
	v_add_u32_e32 v209, 0, v208
	v_mul_u32_u24_e32 v209, 7, v209
	v_add_u32_e32 v230, 6, v209
	v_add_u32_e32 v209, 16, v208
	v_mul_u32_u24_e32 v209, 7, v209
	v_add_u32_e32 v231, 6, v209
	v_add_u32_e32 v209, 32, v208
	v_mul_u32_u24_e32 v209, 7, v209
	v_add_u32_e32 v232, 6, v209
	v_add_u32_e32 v209, 48, v208
	v_mul_u32_u24_e32 v209, 7, v209
	v_add_u32_e32 v233, 6, v209
	v_add_u32_e32 v209, 0x80, v208
	v_mul_u32_u24_e32 v209, 7, v209
	v_add_u32_e32 v234, 6, v209
	v_add_u32_e32 v209, 0x90, v208
	v_mul_u32_u24_e32 v209, 7, v209
	v_add_u32_e32 v235, 6, v209
	v_add_u32_e32 v209, 0xa0, v208
	v_mul_u32_u24_e32 v209, 7, v209
	v_add_u32_e32 v236, 6, v209
	v_add_u32_e32 v209, 0xb0, v208
	v_mul_u32_u24_e32 v209, 7, v209
	v_add_u32_e32 v237, 6, v209
.Lp7a_skip:
	s_barrier
	s_setprio 1
	s_waitcnt lgkmcnt(6)
	v_mfma_scale_f32_16x16x128_f8f6f4 v[92:95], v[0:7], v[174:181], v[92:95], v170, v171 op_sel_hi:[0,0,0]
	v_mfma_scale_f32_16x16x128_f8f6f4 v[88:91], v[8:15], v[174:181], v[88:91], v170, v171 op_sel_hi:[0,0,0]
	s_waitcnt lgkmcnt(4)
	v_mfma_scale_f32_16x16x128_f8f6f4 v[76:79], v[0:7], v[182:189], v[76:79], v170, v171 op_sel_hi:[0,0,0]
	v_mfma_scale_f32_16x16x128_f8f6f4 v[72:75], v[8:15], v[182:189], v[72:75], v170, v171 op_sel_hi:[0,0,0]
	s_waitcnt lgkmcnt(2)
	v_mfma_scale_f32_16x16x128_f8f6f4 v[60:63], v[0:7], v[190:197], v[60:63], v170, v171 op_sel_hi:[0,0,0]
	v_mfma_scale_f32_16x16x128_f8f6f4 v[56:59], v[8:15], v[190:197], v[56:59], v170, v171 op_sel_hi:[0,0,0]
	s_waitcnt lgkmcnt(0)
	v_mfma_scale_f32_16x16x128_f8f6f4 v[44:47], v[0:7], v[198:205], v[44:47], v170, v171 op_sel_hi:[0,0,0]
	v_mfma_scale_f32_16x16x128_f8f6f4 v[40:43], v[8:15], v[198:205], v[40:43], v170, v171 op_sel_hi:[0,0,0]
	s_setprio 0
	s_setprio 1
	v_mfma_scale_f32_16x16x128_f8f6f4 v[84:87], v[16:23], v[174:181], v[84:87], v170, v171 op_sel_hi:[0,0,0]
	v_mfma_scale_f32_16x16x128_f8f6f4 v[80:83], v[24:31], v[174:181], v[80:83], v170, v171 op_sel_hi:[0,0,0]
	v_mfma_scale_f32_16x16x128_f8f6f4 v[68:71], v[16:23], v[182:189], v[68:71], v170, v171 op_sel_hi:[0,0,0]
	v_mfma_scale_f32_16x16x128_f8f6f4 v[64:67], v[24:31], v[182:189], v[64:67], v170, v171 op_sel_hi:[0,0,0]
	v_mfma_scale_f32_16x16x128_f8f6f4 v[52:55], v[16:23], v[190:197], v[52:55], v170, v171 op_sel_hi:[0,0,0]
	v_mfma_scale_f32_16x16x128_f8f6f4 v[48:51], v[24:31], v[190:197], v[48:51], v170, v171 op_sel_hi:[0,0,0]
	v_mfma_scale_f32_16x16x128_f8f6f4 v[36:39], v[16:23], v[198:205], v[36:39], v170, v171 op_sel_hi:[0,0,0]
	v_mfma_scale_f32_16x16x128_f8f6f4 v[32:35], v[24:31], v[198:205], v[32:35], v170, v171 op_sel_hi:[0,0,0]
	s_setprio 0
	s_barrier
	s_add_u32 s75, s75, 0x100
	s_addc_u32 s82, s82, 0
	s_add_u32 s83, s83, 0x100
	s_addc_u32 s84, s84, 0
	s_add_u32 s6, s6, 0x100
	s_addc_u32 s7, s7, 0
	s_cmp_ge_i32 s33, s52
	s_mov_b32 s8, s33
	s_cbranch_scc0 .LBB0_852

;     __device__ __forceinline__ void operator()(const f32x4 (&acc)[2][2][4][2], const Unit& u, int wr, int wc, int fr, int fq) const {
;     ...
;         const int e = tileE[u.pm], lbase = (u.pm - tb[e]) * 256 + wr * 64 + fr, ce = cnt[e];
;         const float ysc = (float)(1 << YSHIFT);
;         int drow[2][4];
; #pragma unroll
;         for (int ai = 0; ai < 2; ++ai)
; #pragma unroll
;             for (int m = 0; m < 4; ++m) { const int local = lbase + ai * HALF + m * 16; drow[ai][m] = (e >= NE) ? (local * 7 + 6) : ((local < ce) ? list2[(size_t)e * LISTCAP + local] : 7 * T); }
.LBB0_855:
	s_nop 15
	s_nop 15
	s_waitcnt vmcnt(0)
	v_mov_b32_e32 v10, v230
	v_mov_b32_e32 v14, v231
	v_mov_b32_e32 v12, v232
	v_mov_b32_e32 v8, v233
	v_mov_b32_e32 v6, v234
	v_mov_b32_e32 v4, v235
	v_mov_b32_e32 v2, v236
	v_mov_b32_e32 v0, v237

; #define PG8_STAGE(bufoff, gbase, voff) do { _Pragma("unroll") for (int _i = 0; _i < 2; ++_i) { unsigned keep_; \
;         asm volatile("s_mov_b32 %0, m0\n\ts_mov_b32 m0, %3\n\ts_nop 0\n\tglobal_load_lds_dwordx4 %1, %2\n\ts_mov_b32 m0, %0" : "=&s"(keep_) : "v"((voff)[_i]), "s"((const char*)(gbase)), "s"(ldsb + (unsigned)((bufoff) + _i * 8192)) : "memory"); } } while (0)
; #define PG8_LDA(dst, b, h) do { _Pragma("unroll") for (int m = 0; m < 4; ++m) _Pragma("unroll") for (int k = 0; k < 2; ++k) dst[m][k] = *(const PG8_LAS bf16x8*)(lds + PG8_SA(b, h) + aoff + m * 2048 + k * 1024); } while (0)
; #define PG8_LDB(dst, b, h) do { _Pragma("unroll") for (int n = 0; n < 2; ++n) _Pragma("unroll") for (int k = 0; k < 2; ++k) dst[n][k] = *(const PG8_LAS bf16x8*)(lds + PG8_SB(b, h) + boff + n * 2048 + k * 1024); } while (0)
; #define PG8_WAIT_V(n) asm volatile("s_waitcnt vmcnt(" #n ")" ::: "memory")
; #define PG8_WAIT_L(n) asm volatile("s_waitcnt lgkmcnt(" #n ")" ::: "memory")
; #define PG8_BAR __builtin_amdgcn_s_barrier()
; #define PG8_SCHED __builtin_amdgcn_sched_barrier(0)
; template <class Epi, class Sched, bool ALIGN_EPI, bool FP8 = false>
; __device__ __forceinline__ void gemm_phase(PG8_LAS unsigned char* lds, const Gemm g, const Sched& S, const Epi& E, const int wid, const int lane) {
;     ...
;         for (int t = 0; t < nt; t += 2) {
;             const bool last = (t == nt - 2);
;             const char* a1 = cA + (size_t)(t + 1) * kstep;
;             const char* a2 = last ? nA : cA + (size_t)(t + 2) * kstep; const char* b2 = last ? nB : cB + (size_t)(t + 2) * kstep;
;             const char* a3 = a2 + kstep; const char* b3 = b2 + kstep;
;             PG8_LDB(B0, 0, 0); PG8_LDB(B1, 0, 1); PG8_SCHED; PG8_LDA(At, 0, 0); PG8_STAGE(PG8_SA(1, 1), a1 + hstepA, vc1);
;             if (GA && last && has_next) { const u32x4 q = *gslot; vc0[0] = q.x; vc0[1] = q.y; vc1[0] = q.z; vc1[1] = q.w; }
;             PG8_WAIT_V(8); PG8_WAIT_L(0); PG8_BAR; PG8_MMA(0, 0, At, B0); PG8_MMA(0, 1, At, B1); PG8_BAR; PG8_SCHED;
;             PG8_LDA(At, 0, 1); PG8_STAGE(PG8_SB(0, 0), b2, voffB); PG8_STAGE(PG8_SB(0, 1), b2 + hstep, voffB); PG8_STAGE(PG8_SA(0, 0), a2, vc0);
;             PG8_WAIT_V(8); PG8_WAIT_L(0); PG8_BAR; PG8_MMA(1, 0, At, B0); PG8_MMA(1, 1, At, B1); PG8_BAR; PG8_SCHED;
.LBB0_1762:
	ds_read_b128 v[24:27], v165
	ds_read_b128 v[28:31], v165 offset:1024
	ds_read_b128 v[16:19], v165 offset:2048
	ds_read_b128 v[20:23], v165 offset:3072
	ds_read_b128 v[8:11], v167
	ds_read_b128 v[12:15], v167 offset:1024
	ds_read_b128 v[0:3], v167 offset:2048
	ds_read_b128 v[4:7], v167 offset:3072
	s_add_i32 s33, s8, 2
	s_cmp_eq_u32 s67, s8
	s_cselect_b32 s36, s28, s75
	s_cselect_b32 s37, s29, s80
	s_cselect_b32 s34, s30, s81
	s_cselect_b32 s35, s31, s82
	s_add_u32 s8, s36, 0x80
	s_addc_u32 s9, s37, 0
	ds_read_b128 v[174:177], v169
	ds_read_b128 v[178:181], v169 offset:1024
	ds_read_b128 v[182:185], v169 offset:2048
	ds_read_b128 v[186:189], v169 offset:3072
	ds_read_b128 v[190:193], v169 offset:4096
	ds_read_b128 v[194:197], v169 offset:5120
	ds_read_b128 v[198:201], v169 offset:6144
	ds_read_b128 v[202:205], v169 offset:7168
	s_mov_b32 m0, s68
	s_nop 0
	global_load_lds_dwordx4 v160, s[6:7]
	s_mov_b32 m0, s69
	s_nop 0
	global_load_lds_dwordx4 v164, s[6:7]
	s_waitcnt vmcnt(8)
	s_waitcnt lgkmcnt(0)
	s_barrier
	s_setprio 1
	s_waitcnt lgkmcnt(6)
	v_mfma_scale_f32_16x16x128_f8f6f4 v[156:159], v[24:31], v[174:181], v[156:159], v170, v171 op_sel_hi:[0,0,0]
	v_mfma_scale_f32_16x16x128_f8f6f4 v[152:155], v[16:23], v[174:181], v[152:155], v170, v171 op_sel_hi:[0,0,0]
	s_waitcnt lgkmcnt(4)
	v_mfma_scale_f32_16x16x128_f8f6f4 v[140:143], v[24:31], v[182:189], v[140:143], v170, v171 op_sel_hi:[0,0,0]
	v_mfma_scale_f32_16x16x128_f8f6f4 v[136:139], v[16:23], v[182:189], v[136:139], v170, v171 op_sel_hi:[0,0,0]
	s_waitcnt lgkmcnt(2)
	v_mfma_scale_f32_16x16x128_f8f6f4 v[124:127], v[24:31], v[190:197], v[124:127], v170, v171 op_sel_hi:[0,0,0]
	v_mfma_scale_f32_16x16x128_f8f6f4 v[120:123], v[16:23], v[190:197], v[120:123], v170, v171 op_sel_hi:[0,0,0]
	s_waitcnt lgkmcnt(0)
	v_mfma_scale_f32_16x16x128_f8f6f4 v[108:111], v[24:31], v[198:205], v[108:111], v170, v171 op_sel_hi:[0,0,0]
	v_mfma_scale_f32_16x16x128_f8f6f4 v[104:107], v[16:23], v[198:205], v[104:107], v170, v171 op_sel_hi:[0,0,0]
	s_setprio 0
	s_setprio 1
	v_mfma_scale_f32_16x16x128_f8f6f4 v[148:151], v[8:15], v[174:181], v[148:151], v170, v171 op_sel_hi:[0,0,0]
	v_mfma_scale_f32_16x16x128_f8f6f4 v[144:147], v[0:7], v[174:181], v[144:147], v170, v171 op_sel_hi:[0,0,0]
	v_mfma_scale_f32_16x16x128_f8f6f4 v[132:135], v[8:15], v[182:189], v[132:135], v170, v171 op_sel_hi:[0,0,0]
	v_mfma_scale_f32_16x16x128_f8f6f4 v[128:131], v[0:7], v[182:189], v[128:131], v170, v171 op_sel_hi:[0,0,0]
	v_mfma_scale_f32_16x16x128_f8f6f4 v[116:119], v[8:15], v[190:197], v[116:119], v170, v171 op_sel_hi:[0,0,0]
	v_mfma_scale_f32_16x16x128_f8f6f4 v[112:115], v[0:7], v[190:197], v[112:115], v170, v171 op_sel_hi:[0,0,0]
	v_mfma_scale_f32_16x16x128_f8f6f4 v[100:103], v[8:15], v[198:205], v[100:103], v170, v171 op_sel_hi:[0,0,0]
	v_mfma_scale_f32_16x16x128_f8f6f4 v[96:99], v[0:7], v[198:205], v[96:99], v170, v171 op_sel_hi:[0,0,0]
	s_setprio 0
	s_barrier
	ds_read_b128 v[174:177], v169 offset:16384
	ds_read_b128 v[178:181], v169 offset:17408
	ds_read_b128 v[182:185], v169 offset:18432
	ds_read_b128 v[186:189], v169 offset:19456
	ds_read_b128 v[190:193], v169 offset:20480
	ds_read_b128 v[194:197], v169 offset:21504
	ds_read_b128 v[198:201], v169 offset:22528
	ds_read_b128 v[202:205], v169 offset:23552
	s_mov_b32 m0, s45
	s_nop 0
	global_load_lds_dwordx4 v162, s[34:35]
	s_mov_b32 m0, s46
	s_nop 0
	global_load_lds_dwordx4 v166, s[34:35]
	s_add_u32 s58, s34, s12
	s_addc_u32 s59, s35, s13
	s_mov_b32 m0, s47
	s_nop 0
	global_load_lds_dwordx4 v162, s[58:59]
	s_mov_b32 m0, s48
	s_nop 0
	global_load_lds_dwordx4 v166, s[58:59]
	s_mov_b32 m0, s40
	s_nop 0
	global_load_lds_dwordx4 v160, s[36:37]
	s_mov_b32 m0, s49
	s_nop 0
	global_load_lds_dwordx4 v164, s[36:37]
	s_waitcnt vmcnt(8)
	s_waitcnt lgkmcnt(0)
	s_barrier
	s_setprio 1
	s_waitcnt lgkmcnt(6)
	v_mfma_scale_f32_16x16x128_f8f6f4 v[92:95], v[24:31], v[174:181], v[92:95], v170, v171 op_sel_hi:[0,0,0]
	v_mfma_scale_f32_16x16x128_f8f6f4 v[88:91], v[16:23], v[174:181], v[88:91], v170, v171 op_sel_hi:[0,0,0]
	s_waitcnt lgkmcnt(4)
	v_mfma_scale_f32_16x16x128_f8f6f4 v[76:79], v[24:31], v[182:189], v[76:79], v170, v171 op_sel_hi:[0,0,0]
	v_mfma_scale_f32_16x16x128_f8f6f4 v[72:75], v[16:23], v[182:189], v[72:75], v170, v171 op_sel_hi:[0,0,0]
	s_waitcnt lgkmcnt(2)
	v_mfma_scale_f32_16x16x128_f8f6f4 v[60:63], v[24:31], v[190:197], v[60:63], v170, v171 op_sel_hi:[0,0,0]
	v_mfma_scale_f32_16x16x128_f8f6f4 v[56:59], v[16:23], v[190:197], v[56:59], v170, v171 op_sel_hi:[0,0,0]
	s_waitcnt lgkmcnt(0)
	v_mfma_scale_f32_16x16x128_f8f6f4 v[44:47], v[24:31], v[198:205], v[44:47], v170, v171 op_sel_hi:[0,0,0]
	v_mfma_scale_f32_16x16x128_f8f6f4 v[40:43], v[16:23], v[198:205], v[40:43], v170, v171 op_sel_hi:[0,0,0]
	s_setprio 0
	s_setprio 1
	v_mfma_scale_f32_16x16x128_f8f6f4 v[84:87], v[8:15], v[174:181], v[84:87], v170, v171 op_sel_hi:[0,0,0]
	v_mfma_scale_f32_16x16x128_f8f6f4 v[80:83], v[0:7], v[174:181], v[80:83], v170, v171 op_sel_hi:[0,0,0]
	v_mfma_scale_f32_16x16x128_f8f6f4 v[68:71], v[8:15], v[182:189], v[68:71], v170, v171 op_sel_hi:[0,0,0]
	v_mfma_scale_f32_16x16x128_f8f6f4 v[64:67], v[0:7], v[182:189], v[64:67], v170, v171 op_sel_hi:[0,0,0]
	v_mfma_scale_f32_16x16x128_f8f6f4 v[52:55], v[8:15], v[190:197], v[52:55], v170, v171 op_sel_hi:[0,0,0]
	v_mfma_scale_f32_16x16x128_f8f6f4 v[48:51], v[0:7], v[190:197], v[48:51], v170, v171 op_sel_hi:[0,0,0]
	v_mfma_scale_f32_16x16x128_f8f6f4 v[36:39], v[8:15], v[198:205], v[36:39], v170, v171 op_sel_hi:[0,0,0]
	v_mfma_scale_f32_16x16x128_f8f6f4 v[32:35], v[0:7], v[198:205], v[32:35], v170, v171 op_sel_hi:[0,0,0]
	s_setprio 0
	s_barrier
; #define PG8_STAGE(bufoff, gbase, voff) do { _Pragma("unroll") for (int _i = 0; _i < 2; ++_i) { unsigned keep_; \
;         asm volatile("s_mov_b32 %0, m0\n\ts_mov_b32 m0, %3\n\ts_nop 0\n\tglobal_load_lds_dwordx4 %1, %2\n\ts_mov_b32 m0, %0" : "=&s"(keep_) : "v"((voff)[_i]), "s"((const char*)(gbase)), "s"(ldsb + (unsigned)((bufoff) + _i * 8192)) : "memory"); } } while (0)
; #define PG8_LDA(dst, b, h) do { _Pragma("unroll") for (int m = 0; m < 4; ++m) _Pragma("unroll") for (int k = 0; k < 2; ++k) dst[m][k] = *(const PG8_LAS bf16x8*)(lds + PG8_SA(b, h) + aoff + m * 2048 + k * 1024); } while (0)
; #define PG8_LDB(dst, b, h) do { _Pragma("unroll") for (int n = 0; n < 2; ++n) _Pragma("unroll") for (int k = 0; k < 2; ++k) dst[n][k] = *(const PG8_LAS bf16x8*)(lds + PG8_SB(b, h) + boff + n * 2048 + k * 1024); } while (0)
; #define PG8_WAIT_V(n) asm volatile("s_waitcnt vmcnt(" #n ")" ::: "memory")
; #define PG8_WAIT_L(n) asm volatile("s_waitcnt lgkmcnt(" #n ")" ::: "memory")
; #define PG8_BAR __builtin_amdgcn_s_barrier()
; #define PG8_SCHED __builtin_amdgcn_sched_barrier(0)
; template <class Epi, class Sched, bool ALIGN_EPI, bool FP8 = false>
; __device__ __forceinline__ void gemm_phase(PG8_LAS unsigned char* lds, const Gemm g, const Sched& S, const Epi& E, const int wid, const int lane) {
;     ...
;             PG8_LDB(B0, 1, 0); PG8_LDB(B1, 1, 1); PG8_SCHED; PG8_LDA(At, 1, 0); PG8_STAGE(PG8_SA(0, 1), a2 + hstepA, vc1);
;             PG8_WAIT_V(8); PG8_WAIT_L(0); PG8_BAR; PG8_MMA(0, 0, At, B0); PG8_MMA(0, 1, At, B1); PG8_BAR; PG8_SCHED;
;             PG8_LDA(At, 1, 1); PG8_STAGE(PG8_SB(1, 0), b3, voffB); PG8_STAGE(PG8_SB(1, 1), b3 + hstep, voffB); PG8_STAGE(PG8_SA(1, 0), a3, vc0);
;     __device__ __forceinline__ void operator()(const f32x4 (&acc)[2][2][4][2], const Unit& u, int wr, int wc, int fr, int fq) const {
;         const int col0 = (u.pn & 7) * 256 + wc * 64 + 16 * fq;
;         const int e = tileE[u.pm], lbase = (u.pm - tb[e]) * 256 + wr * 64 + fr, ce = cnt[e];
;         const float ysc = (float)(1 << YSHIFT);
;         int drow[2][4];
; #pragma unroll
;         for (int ai = 0; ai < 2; ++ai)
; #pragma unroll
;             for (int m = 0; m < 4; ++m) { const int local = lbase + ai * HALF + m * 16; drow[ai][m] = (e >= NE) ? (local * 7 + 6) : ((local < ce) ? list2[(size_t)e * LISTCAP + local] : 7 * T); }
	ds_read_b128 v[0:3], v172
	ds_read_b128 v[4:7], v172 offset:1024
	ds_read_b128 v[8:11], v172 offset:2048
	ds_read_b128 v[12:15], v172 offset:3072
	ds_read_b128 v[16:19], v173
	ds_read_b128 v[20:23], v173 offset:1024
	ds_read_b128 v[24:27], v173 offset:2048
	ds_read_b128 v[28:31], v173 offset:3072
	ds_read_b128 v[174:177], v169 offset:32768
	ds_read_b128 v[178:181], v169 offset:33792
	ds_read_b128 v[182:185], v169 offset:34816
	ds_read_b128 v[186:189], v169 offset:35840
	ds_read_b128 v[190:193], v169 offset:36864
	ds_read_b128 v[194:197], v169 offset:37888
	ds_read_b128 v[198:201], v169 offset:38912
	ds_read_b128 v[202:205], v169 offset:39936
	s_add_u32 s36, s36, s12
	s_addc_u32 s37, s37, s13
	s_mov_b32 m0, s50
	s_nop 0
	global_load_lds_dwordx4 v160, s[36:37]
	s_mov_b32 m0, s51
	s_nop 0
	global_load_lds_dwordx4 v164, s[36:37]
	s_waitcnt vmcnt(8)
	s_waitcnt lgkmcnt(0)
	s_barrier
	s_setprio 1
	s_waitcnt lgkmcnt(6)
	v_mfma_scale_f32_16x16x128_f8f6f4 v[156:159], v[0:7], v[174:181], v[156:159], v170, v171 op_sel_hi:[0,0,0]
	v_mfma_scale_f32_16x16x128_f8f6f4 v[152:155], v[8:15], v[174:181], v[152:155], v170, v171 op_sel_hi:[0,0,0]
	s_waitcnt lgkmcnt(4)
	v_mfma_scale_f32_16x16x128_f8f6f4 v[140:143], v[0:7], v[182:189], v[140:143], v170, v171 op_sel_hi:[0,0,0]
	v_mfma_scale_f32_16x16x128_f8f6f4 v[136:139], v[8:15], v[182:189], v[136:139], v170, v171 op_sel_hi:[0,0,0]
	s_waitcnt lgkmcnt(2)
	v_mfma_scale_f32_16x16x128_f8f6f4 v[124:127], v[0:7], v[190:197], v[124:127], v170, v171 op_sel_hi:[0,0,0]
	v_mfma_scale_f32_16x16x128_f8f6f4 v[120:123], v[8:15], v[190:197], v[120:123], v170, v171 op_sel_hi:[0,0,0]
	s_waitcnt lgkmcnt(0)
	v_mfma_scale_f32_16x16x128_f8f6f4 v[108:111], v[0:7], v[198:205], v[108:111], v170, v171 op_sel_hi:[0,0,0]
	v_mfma_scale_f32_16x16x128_f8f6f4 v[104:107], v[8:15], v[198:205], v[104:107], v170, v171 op_sel_hi:[0,0,0]
	s_setprio 0
	s_setprio 1
	v_mfma_scale_f32_16x16x128_f8f6f4 v[148:151], v[16:23], v[174:181], v[148:151], v170, v171 op_sel_hi:[0,0,0]
	v_mfma_scale_f32_16x16x128_f8f6f4 v[144:147], v[24:31], v[174:181], v[144:147], v170, v171 op_sel_hi:[0,0,0]
	v_mfma_scale_f32_16x16x128_f8f6f4 v[132:135], v[16:23], v[182:189], v[132:135], v170, v171 op_sel_hi:[0,0,0]
	v_mfma_scale_f32_16x16x128_f8f6f4 v[128:131], v[24:31], v[182:189], v[128:131], v170, v171 op_sel_hi:[0,0,0]
	v_mfma_scale_f32_16x16x128_f8f6f4 v[116:119], v[16:23], v[190:197], v[116:119], v170, v171 op_sel_hi:[0,0,0]
	v_mfma_scale_f32_16x16x128_f8f6f4 v[112:115], v[24:31], v[190:197], v[112:115], v170, v171 op_sel_hi:[0,0,0]
	v_mfma_scale_f32_16x16x128_f8f6f4 v[100:103], v[16:23], v[198:205], v[100:103], v170, v171 op_sel_hi:[0,0,0]
	v_mfma_scale_f32_16x16x128_f8f6f4 v[96:99], v[24:31], v[198:205], v[96:99], v170, v171 op_sel_hi:[0,0,0]
	s_setprio 0
	s_barrier
	ds_read_b128 v[174:177], v169 offset:49152
	ds_read_b128 v[178:181], v169 offset:50176
	ds_read_b128 v[182:185], v169 offset:51200
	ds_read_b128 v[186:189], v169 offset:52224
	ds_read_b128 v[190:193], v169 offset:53248
	ds_read_b128 v[194:197], v169 offset:54272
	ds_read_b128 v[198:201], v169 offset:55296
	ds_read_b128 v[202:205], v169 offset:56320
	s_add_u32 s34, s34, 0x80
	s_addc_u32 s35, s35, 0
	s_mov_b32 m0, s53
	s_nop 0
	global_load_lds_dwordx4 v162, s[34:35]
	s_mov_b32 m0, s54
	s_nop 0
	global_load_lds_dwordx4 v166, s[34:35]
	s_add_u32 s34, s34, s12
	s_addc_u32 s35, s35, s13
	s_mov_b32 m0, s65
	s_nop 0
	global_load_lds_dwordx4 v162, s[34:35]
	s_mov_b32 m0, s66
	s_nop 0
	global_load_lds_dwordx4 v166, s[34:35]
	s_mov_b32 m0, s55
	s_nop 0
	global_load_lds_dwordx4 v160, s[8:9]
	s_mov_b32 m0, s64
	s_nop 0
	global_load_lds_dwordx4 v164, s[8:9]
	s_waitcnt vmcnt(8)
	s_waitcnt lgkmcnt(0)
	s_cmp_lt_i32 s33, s52
	s_cbranch_scc1 .Lp7b_skip
	s_lshl_b32 s98, s74, 2
	s_add_i32 s98, s98, 0x20800
	v_mov_b32_e32 v206, s98
	ds_read_b32 v207, v206
	s_waitcnt lgkmcnt(0)
	s_nop 0
	v_readfirstlane_b32 s99, v207
	s_nop 3
	s_lshl_b32 s98, s99, 2
	s_add_i32 s100, s98, 0x21000
	s_add_i32 s98, s98, 0x21200
	v_mov_b32_e32 v206, s100
	v_mov_b32_e32 v207, s98
	ds_read_b32 v206, v206
	ds_read_b32 v207, v207
	s_waitcnt lgkmcnt(0)
	v_sub_u32_e32 v206, s74, v206
	v_lshl_add_u32 v208, v206, 8, v161
	s_cmp_gt_i32 s99, 63
	s_cbranch_scc1 .Lp7b_shared
	s_mov_b32 s100, s99
	s_ashr_i32 s101, s99, 31
	s_lshl_b64 s[100:101], s[100:101], 16
	s_add_u32 s100, s20, s100
	s_addc_u32 s101, s21, s101
	v_add_u32_e32 v209, 0, v208
	v_cmp_lt_i32_e32 vcc, v209, v207
	v_lshlrev_b32_e32 v238, 2, v209
	v_mov_b32_e32 v230, 0x1c000
	s_and_saveexec_b64 s[98:99], vcc
	s_cbranch_execz .Lp7b_g0
	global_load_dword v230, v238, s[100:101]

; #define PG8_WAIT_V(n) asm volatile("s_waitcnt vmcnt(" #n ")" ::: "memory")
; #define PG8_WAIT_L(n) asm volatile("s_waitcnt lgkmcnt(" #n ")" ::: "memory")
; #define PG8_BAR __builtin_amdgcn_s_barrier()
; #define PG8_SCHED __builtin_amdgcn_sched_barrier(0)
; template <class Epi, class Sched, bool ALIGN_EPI, bool FP8 = false>
; __device__ __forceinline__ void gemm_phase(PG8_LAS unsigned char* lds, const Gemm g, const Sched& S, const Epi& E, const int wid, const int lane) {
;     ...
;             PG8_WAIT_V(8); PG8_WAIT_L(0); PG8_BAR; PG8_MMA(1, 0, At, B0); PG8_MMA(1, 1, At, B1); PG8_BAR; PG8_SCHED;
;         }
.Lp7b_skip:
	s_barrier
	s_setprio 1
	s_waitcnt lgkmcnt(6)
	v_mfma_scale_f32_16x16x128_f8f6f4 v[92:95], v[0:7], v[174:181], v[92:95], v170, v171 op_sel_hi:[0,0,0]
	v_mfma_scale_f32_16x16x128_f8f6f4 v[88:91], v[8:15], v[174:181], v[88:91], v170, v171 op_sel_hi:[0,0,0]
	s_waitcnt lgkmcnt(4)
	v_mfma_scale_f32_16x16x128_f8f6f4 v[76:79], v[0:7], v[182:189], v[76:79], v170, v171 op_sel_hi:[0,0,0]
	v_mfma_scale_f32_16x16x128_f8f6f4 v[72:75], v[8:15], v[182:189], v[72:75], v170, v171 op_sel_hi:[0,0,0]
	s_waitcnt lgkmcnt(2)
	v_mfma_scale_f32_16x16x128_f8f6f4 v[60:63], v[0:7], v[190:197], v[60:63], v170, v171 op_sel_hi:[0,0,0]
	v_mfma_scale_f32_16x16x128_f8f6f4 v[56:59], v[8:15], v[190:197], v[56:59], v170, v171 op_sel_hi:[0,0,0]
	s_waitcnt lgkmcnt(0)
	v_mfma_scale_f32_16x16x128_f8f6f4 v[44:47], v[0:7], v[198:205], v[44:47], v170, v171 op_sel_hi:[0,0,0]
	v_mfma_scale_f32_16x16x128_f8f6f4 v[40:43], v[8:15], v[198:205], v[40:43], v170, v171 op_sel_hi:[0,0,0]
	s_setprio 0
	s_setprio 1
	v_mfma_scale_f32_16x16x128_f8f6f4 v[84:87], v[16:23], v[174:181], v[84:87], v170, v171 op_sel_hi:[0,0,0]
	v_mfma_scale_f32_16x16x128_f8f6f4 v[80:83], v[24:31], v[174:181], v[80:83], v170, v171 op_sel_hi:[0,0,0]
	v_mfma_scale_f32_16x16x128_f8f6f4 v[68:71], v[16:23], v[182:189], v[68:71], v170, v171 op_sel_hi:[0,0,0]
	v_mfma_scale_f32_16x16x128_f8f6f4 v[64:67], v[24:31], v[182:189], v[64:67], v170, v171 op_sel_hi:[0,0,0]
	v_mfma_scale_f32_16x16x128_f8f6f4 v[52:55], v[16:23], v[190:197], v[52:55], v170, v171 op_sel_hi:[0,0,0]
	v_mfma_scale_f32_16x16x128_f8f6f4 v[48:51], v[24:31], v[190:197], v[48:51], v170, v171 op_sel_hi:[0,0,0]
	v_mfma_scale_f32_16x16x128_f8f6f4 v[36:39], v[16:23], v[198:205], v[36:39], v170, v171 op_sel_hi:[0,0,0]
	v_mfma_scale_f32_16x16x128_f8f6f4 v[32:35], v[24:31], v[198:205], v[32:35], v170, v171 op_sel_hi:[0,0,0]
	s_setprio 0
	s_barrier
	s_add_u32 s75, s75, 0x100
	s_addc_u32 s80, s80, 0
	s_add_u32 s81, s81, 0x100
	s_addc_u32 s82, s82, 0
	s_add_u32 s6, s6, 0x100
	s_addc_u32 s7, s7, 0
	s_cmp_ge_i32 s33, s52
	s_mov_b32 s8, s33
	s_cbranch_scc0 .LBB0_1762
